# in-projection K-loop: a unit's first two staging waits skip the previous unit's epilogue stores (vmcnt 24, or 16 after the g_fox/f_logit tile)
# baseline (speedup 1.0000x reference)
; #define PG8_STAGE(bufoff, gbase, voff) do { _Pragma("unroll") for (int _i = 0; _i < 2; ++_i) \
;         __builtin_amdgcn_global_load_lds((const unsigned*)((const char*)(gbase) + (voff)[_i]), (PG8_LAS unsigned*)(lds + (bufoff) + ldsw + _i * 8192), 16, 0, 0); } while (0)
; #define PG8_WAIT_V(n) asm volatile("s_waitcnt vmcnt(" #n ")" ::: "memory")
; #define PG8_BAR __builtin_amdgcn_s_barrier()
; template <class Epi, class Sched, bool ALIGN_EPI = false, bool SP2 = false>
; __device__ __forceinline__ void gemm_phase(PG8_LAS unsigned char* lds, const Gemm g, const Sched& S, const Epi& E, const int tid) {
;     const int wid = __builtin_amdgcn_readfirstlane(tid >> 6), lane = tid & 63, wr = wid >> 2, wc = wid & 3, fr = lane & 15, fq = lane >> 4;
;     const int K = g.K, nt = K / BK;
;     unsigned voffA[2], voffB[2];
; #pragma unroll
;     for (int i = 0; i < 2; ++i) { int R, C; stage_rc(tid * 16 + i * 8192, R, C); const int Rb = Epi::PERM ? ((R & ~31) + perm32(R & 31)) : R;
;         voffA[i] = (unsigned)(R * g.lda + C) * 2u; voffB[i] = (unsigned)(Rb * K + C) * 2u; }
;     const size_t kstep = (size_t)(BK * 2);
;     const size_t hstep = (size_t)HALF * K * 2;
;     const size_t tstep = 2 * hstep;
;     const size_t hstepA = (size_t)HALF * g.lda * 2, tstepA = 2 * hstepA; const long padj = g.padj;
;     ...
;     const unsigned ldsw = (unsigned)wid * 1024u;
;     const int aoff = lds_byte(wr * 64 + fr, fq * 8), boff = lds_byte(wc * 32 + fr, fq * 8);
;     ...
;         PG8_WAIT_V(2); PG8_BAR;
;         PG8_STAGE(PG8_SB(1, 0), cB + kstep, voffB); PG8_STAGE(PG8_SA(1, 0), cA + kstep, voffA); PG8_STAGE(PG8_SB(1, 1), cB + hstep + kstep, voffB);
;         PG8_WAIT_V(6); PG8_BAR;
.LBB0_550:
	v_readlane_b32 s6, v254, 20
	v_readlane_b32 s7, v254, 21
	s_ashr_i32 s7, s6, 31
	v_readlane_b32 s52, v253, 54
	s_lshl_b64 s[6:7], s[6:7], 2
	v_readlane_b32 s58, v253, 60
	v_mov_b32_e32 v149, v1
	v_readlane_b32 s59, v253, 61
	s_add_u32 s6, s58, s6
	v_lshl_add_u64 v[8:9], s[28:29], 0, v[148:149]
	v_mov_b32_e32 v153, v1
	v_readlane_b32 s53, v253, 55
	s_addc_u32 s7, s59, s7
	s_add_i32 s52, s44, 0x18000
	v_lshl_add_u64 v[10:11], s[28:29], 0, v[152:153]
	v_mov_b32_e32 v147, v1
	v_readlane_b32 s54, v253, 56
	v_readlane_b32 s55, v253, 57
	s_and_b32 s18, s10, 3
	v_lshl_add_u64 v[8:9], v[8:9], 0, s[86:87]
	s_mov_b32 m0, s52
	s_add_i32 s53, s44, 0x1a000
	v_lshl_add_u64 v[12:13], s[30:31], 0, v[146:147]
	v_mov_b32_e32 v151, v1
	s_lshl_b32 s14, s11, 6
	s_lshl_b32 s5, s11, 13
	s_lshl_b32 s9, s18, 12
	s_waitcnt vmcnt(2)
	s_barrier
	global_load_lds_dwordx4 v[8:9], off
	v_lshl_add_u64 v[8:9], v[10:11], 0, s[86:87]
	s_mov_b32 m0, s53
	s_add_i32 s54, s44, 0x8000
	s_add_i32 s55, s44, 0xa000
	v_lshl_add_u64 v[14:15], s[30:31], 0, v[150:151]
	v_readlane_b32 s56, v253, 58
	global_load_lds_dwordx4 v[8:9], off
	v_lshl_add_u64 v[8:9], v[12:13], 0, s[86:87]
	s_mov_b32 m0, s54
	s_add_u32 s12, s28, 0x40080
	v_readlane_b32 s57, v253, 59
	global_load_lds_dwordx4 v[8:9], off
	v_lshl_add_u64 v[8:9], v[14:15], 0, s[86:87]
	s_mov_b32 m0, s55
	s_addc_u32 s13, s29, 0
	s_add_i32 s56, s44, 0x1c000
	global_load_lds_dwordx4 v[8:9], off
	v_lshl_add_u64 v[8:9], s[12:13], 0, v[148:149]
	s_mov_b32 m0, s56
	s_add_i32 s57, s44, 0x1e000
	global_load_lds_dwordx4 v[8:9], off
	v_lshl_add_u64 v[8:9], s[12:13], 0, v[152:153]
	s_mov_b32 m0, s57
	v_lshrrev_b32_e32 v7, 4, v232
	global_load_lds_dwordx4 v[8:9], off
	v_and_b32_e32 v8, 15, v232
	v_bfe_u32 v9, v232, 4, 2
	v_lshlrev_b32_e32 v11, 4, v9
	v_lshlrev_b32_e32 v13, 2, v8
	v_lshlrev_b32_e32 v10, 3, v9
	v_lshl_or_b32 v12, v8, 6, v11
	v_and_b32_e32 v14, 32, v13
	s_cmpk_lt_u32 s8, 0x100
	v_bitop3_b32 v7, s10, v7, 3 bitop3:0xa8
	v_or_b32_e32 v163, s14, v8
	v_bitop3_b32 v167, s9, v12, v14 bitop3:0xf6
	s_cselect_b64 s[8:9], -1, 0
	v_cmp_eq_u32_e64 s[34:35], 0, v7
	s_lshl_b32 s10, s18, 7
	v_cmp_eq_u32_e64 s[36:37], 0, v8
	v_or_b32_e32 v7, s14, v10
	v_and_b32_e32 v8, 64, v214
	v_add_u32_e32 v171, s10, v7
	v_xor_b32_e32 v7, 32, v214
	v_add_u32_e32 v8, 64, v8
	v_cmp_lt_i32_e32 vcc, v7, v8
	v_or_b32_e32 v175, s10, v11
	s_lshl_b32 s10, s11, 8
	v_cndmask_b32_e32 v7, v214, v7, vcc
	v_lshlrev_b32_e32 v195, 2, v7
	v_xor_b32_e32 v7, 1, v214
	v_cmp_lt_i32_e32 vcc, v7, v8
	s_add_i32 s10, s10, 0x20200
	v_or_b32_e32 v181, s10, v13
	v_cndmask_b32_e32 v7, v214, v7, vcc
	v_lshlrev_b32_e32 v233, 2, v7
	v_xor_b32_e32 v7, 2, v214
	v_cmp_lt_i32_e32 vcc, v7, v8
	s_lshl_b32 s10, s18, 8
	s_add_i32 s10, s10, 0x22200
	v_cndmask_b32_e32 v7, v214, v7, vcc
	v_lshlrev_b32_e32 v234, 2, v7
	v_xor_b32_e32 v7, 4, v214
	v_cmp_lt_i32_e32 vcc, v7, v8
	v_lshl_or_b32 v187, v9, 5, s10
	s_add_u32 s10, s74, 0x18000000
	v_cndmask_b32_e32 v7, v214, v7, vcc
	v_lshlrev_b32_e32 v235, 2, v7
	v_xor_b32_e32 v7, 8, v214
	v_cmp_lt_i32_e32 vcc, v7, v8
	s_addc_u32 s11, s75, 0
	s_add_u32 s12, s74, 0x3600000
	v_cndmask_b32_e32 v7, v214, v7, vcc
	v_lshlrev_b32_e32 v236, 2, v7
	v_lshlrev_b32_e32 v7, 14, v4
	v_and_b32_e32 v7, 0xffff8000, v7
	v_lshl_add_u32 v5, v5, 11, v7
	v_and_b32_e32 v4, 1, v4
	v_lshl_or_b32 v4, v4, 6, v5
	s_addc_u32 s13, s75, 0
	v_lshl_add_u32 v154, v6, 1, v4
	v_lshlrev_b32_e32 v4, 14, v0
	s_add_u32 s14, s74, 0x8000000
	v_and_b32_e32 v4, 0xffff8000, v4
	s_waitcnt vmcnt(6)
	s_addc_u32 s15, s75, 0
	v_lshl_add_u32 v2, v2, 11, v4
	v_and_b32_e32 v0, 1, v0
	s_add_u32 s16, s74, 0x3700000
	v_lshl_or_b32 v0, v0, 6, v2
	v_bitop3_b32 v165, v12, s5, v14 bitop3:0xde
	s_mov_b32 s5, 0
	s_addc_u32 s17, s75, 0
	v_lshl_or_b32 v237, s18, 5, v10
	v_lshl_or_b32 v238, s18, 6, v10
	v_mov_b32_e32 v155, v1
	v_lshl_add_u32 v156, v3, 1, v0
	v_mov_b32_e32 v157, v1
	v_readlane_b32 s60, v253, 62
	v_readlane_b32 s61, v253, 63
	v_readlane_b32 s62, v254, 0
	v_readlane_b32 s63, v254, 1
	v_readlane_b32 s64, v254, 2
	v_readlane_b32 s65, v254, 3
	v_readlane_b32 s66, v254, 4
	v_readlane_b32 s67, v254, 5
	s_barrier
	s_mov_b32 s100, 0
	s_branch .LBB0_553

; #define PG8_STAGE(bufoff, gbase, voff) do { _Pragma("unroll") for (int _i = 0; _i < 2; ++_i) \
;         __builtin_amdgcn_global_load_lds((const unsigned*)((const char*)(gbase) + (voff)[_i]), (PG8_LAS unsigned*)(lds + (bufoff) + ldsw + _i * 8192), 16, 0, 0); } while (0)
; #define PG8_LDA(dst, b, h) do { _Pragma("unroll") for (int m = 0; m < 4; ++m) _Pragma("unroll") for (int k = 0; k < 2; ++k) dst[m][k] = *(const PG8_LAS bf16x8*)(lds + PG8_SA(b, h) + aoff + m * 2048 + k * 1024); } while (0)
; #define PG8_LDB(dst, b, h) do { _Pragma("unroll") for (int n = 0; n < 2; ++n) _Pragma("unroll") for (int k = 0; k < 2; ++k) dst[n][k] = *(const PG8_LAS bf16x8*)(lds + PG8_SB(b, h) + boff + n * 2048 + k * 1024); } while (0)
; #define PG8_MMA(ai, bj, At, Bt) do { __builtin_amdgcn_s_setprio(1); _Pragma("unroll") for (int m = 0; m < 4; ++m) _Pragma("unroll") for (int n = 0; n < 2; ++n) _Pragma("unroll") for (int k = 0; k < 2; ++k) \
;         acc[ai][bj][m][n] = __builtin_amdgcn_mfma_f32_16x16x32_bf16(Bt[n][k], At[m][k], acc[ai][bj][m][n], 0, 0, 0); __builtin_amdgcn_s_setprio(0); } while (0)
; #define PG8_WAIT_V(n) asm volatile("s_waitcnt vmcnt(" #n ")" ::: "memory")
; #define PG8_WAIT_L(n) asm volatile("s_waitcnt lgkmcnt(" #n ")" ::: "memory")
; #define PG8_BAR __builtin_amdgcn_s_barrier()
; template <class Epi, class Sched, bool ALIGN_EPI = false, bool SP2 = false>
; __device__ __forceinline__ void gemm_phase(PG8_LAS unsigned char* lds, const Gemm g, const Sched& S, const Epi& E, const int tid) {
;     ...
;         const char* nA = has_next ? (const char*)g.A + (size_t)nxt.pm * tstepA : cA; const char* nB = has_next ? (const char*)g.Bt + (size_t)nxt.pn * tstep : cB;
;         for (int t = 0; t < nt; t += 2) {
;             const bool last = (t == nt - 2);
;             const char* a1 = cA + PG8_KOFFA(t + 1);
;             const char* a2 = last ? nA : cA + PG8_KOFFA(t + 2); const char* b2 = last ? nB : cB + (size_t)(t + 2) * kstep;
;             const char* a3 = a2 + kstep; const char* b3 = b2 + kstep;
;             if (last && has_next) S.a_ready(nxt);
;             if constexpr (SP2) {
;             PG8_LDB(B0, 0, 0); PG8_LDB(B1, 0, 1); PG8_SCHED; PG8_LDA(At, 0, 0); PG8_STAGE(PG8_SA(1, 1), a1 + hstepA, voffA);
;             PG8_WAIT_V(8); PG8_WAIT_L(0); PG8_BAR; PG8_MMA(0, 0, At, B0); PG8_MMA(0, 1, At, B1); PG8_BAR; PG8_SCHED;
.LBB0_556:
	v_or_b32_e32 v0, 0x10000, v167
	v_add_u32_e32 v134, 0x10400, v167
	ds_read_b128 v[130:133], v0
	ds_read_b128 v[134:137], v134
	v_add_u32_e32 v0, 0x10800, v167
	v_add_u32_e32 v142, 0x10c00, v167
	ds_read_b128 v[138:141], v0
	ds_read_b128 v[142:145], v142
	v_or_b32_e32 v0, 0x14000, v167
	v_add_u32_e32 v162, 0x14400, v167
	ds_read_b128 v[158:161], v0
	ds_read_b128 v[176:179], v162
	v_add_u32_e32 v0, 0x14800, v167
	v_add_u32_e32 v162, 0x14c00, v167
	ds_read_b128 v[182:185], v0
	ds_read_b128 v[196:199], v162
	s_add_u32 s30, s28, 0xfffc0080
	s_addc_u32 s31, s29, -1
	s_cmp_eq_u32 s61, 12
	s_cselect_b32 s41, s21, s31
	s_cselect_b32 s40, s27, s30
	s_cselect_b32 s31, s19, s60
	s_cselect_b32 s30, s33, s59
	v_lshl_add_u64 v[168:169], s[28:29], 0, v[156:157]
	s_add_i32 m0, s44, 0xc000
	ds_read_b128 v[200:203], v165
	ds_read_b128 v[204:207], v165 offset:1024
	ds_read_b128 v[208:211], v165 offset:2048
	ds_read_b128 v[240:243], v165 offset:3072
	ds_read_b128 v[244:247], v165 offset:4096
	ds_read_b128 v[248:251], v165 offset:5120
	ds_read_b128 v[218:221], v165 offset:6144
	ds_read_b128 v[188:191], v165 offset:7168
	global_load_lds_dwordx4 v[168:169], off
	v_lshl_add_u64 v[168:169], s[28:29], 0, v[154:155]
	s_add_i32 m0, s44, 0xe000
	s_nop 0
	global_load_lds_dwordx4 v[168:169], off
	s_cmp_eq_u32 s100, 0
	s_cbranch_scc1 .Lin_w8_0
	s_add_i32 s100, s100, -1
	s_cmp_eq_u32 s101, 24
	s_cbranch_scc1 .Lin_w24_0
	s_waitcnt vmcnt(16)
	s_branch .Lin_wd_0
.Lin_w24_0:
	s_waitcnt vmcnt(24)
	s_branch .Lin_wd_0

; #define PG8_STAGE(bufoff, gbase, voff) do { _Pragma("unroll") for (int _i = 0; _i < 2; ++_i) \
;         __builtin_amdgcn_global_load_lds((const unsigned*)((const char*)(gbase) + (voff)[_i]), (PG8_LAS unsigned*)(lds + (bufoff) + ldsw + _i * 8192), 16, 0, 0); } while (0)
; #define PG8_LDA(dst, b, h) do { _Pragma("unroll") for (int m = 0; m < 4; ++m) _Pragma("unroll") for (int k = 0; k < 2; ++k) dst[m][k] = *(const PG8_LAS bf16x8*)(lds + PG8_SA(b, h) + aoff + m * 2048 + k * 1024); } while (0)
; #define PG8_MMA(ai, bj, At, Bt) do { __builtin_amdgcn_s_setprio(1); _Pragma("unroll") for (int m = 0; m < 4; ++m) _Pragma("unroll") for (int n = 0; n < 2; ++n) _Pragma("unroll") for (int k = 0; k < 2; ++k) \
;         acc[ai][bj][m][n] = __builtin_amdgcn_mfma_f32_16x16x32_bf16(Bt[n][k], At[m][k], acc[ai][bj][m][n], 0, 0, 0); __builtin_amdgcn_s_setprio(0); } while (0)
; #define PG8_WAIT_V(n) asm volatile("s_waitcnt vmcnt(" #n ")" ::: "memory")
; #define PG8_WAIT_L(n) asm volatile("s_waitcnt lgkmcnt(" #n ")" ::: "memory")
; #define PG8_BAR __builtin_amdgcn_s_barrier()
; #define PG8_SCHED __builtin_amdgcn_sched_barrier(0)
; template <class Epi, class Sched, bool ALIGN_EPI = false, bool SP2 = false>
; __device__ __forceinline__ void gemm_phase(PG8_LAS unsigned char* lds, const Gemm g, const Sched& S, const Epi& E, const int tid) {
;     ...
;             PG8_WAIT_V(8); PG8_WAIT_L(0); PG8_BAR; PG8_MMA(0, 0, At, B0); PG8_MMA(0, 1, At, B1); PG8_BAR; PG8_SCHED;
;             PG8_LDA(At, 0, 1); PG8_STAGE(PG8_SB(0, 0), b2, voffB); PG8_STAGE(PG8_SB(0, 1), b2 + hstep, voffB); PG8_STAGE(PG8_SA(0, 0), a2, voffA);
;             PG8_WAIT_V(8); PG8_WAIT_L(0); PG8_BAR; PG8_MMA(1, 0, At, B0); PG8_MMA(1, 1, At, B1); PG8_BAR; PG8_SCHED;
.Lin_wd_0:
	s_waitcnt lgkmcnt(0)
	s_barrier
	s_setprio 1
	s_waitcnt lgkmcnt(0)
	v_mfma_f32_16x16x32_bf16 v[126:129], v[130:133], v[200:203], v[126:129]
	v_mfma_f32_16x16x32_bf16 v[122:125], v[138:141], v[200:203], v[122:125]
	v_mfma_f32_16x16x32_bf16 v[110:113], v[130:133], v[208:211], v[110:113]
	v_mfma_f32_16x16x32_bf16 v[106:109], v[138:141], v[208:211], v[106:109]
	v_mfma_f32_16x16x32_bf16 v[94:97], v[130:133], v[244:247], v[94:97]
	v_mfma_f32_16x16x32_bf16 v[90:93], v[138:141], v[244:247], v[90:93]
	v_mfma_f32_16x16x32_bf16 v[78:81], v[130:133], v[218:221], v[78:81]
	v_mfma_f32_16x16x32_bf16 v[74:77], v[138:141], v[218:221], v[74:77]
	v_mfma_f32_16x16x32_bf16 v[126:129], v[134:137], v[204:207], v[126:129]
	v_mfma_f32_16x16x32_bf16 v[122:125], v[142:145], v[204:207], v[122:125]
	v_mfma_f32_16x16x32_bf16 v[110:113], v[134:137], v[240:243], v[110:113]
	v_mfma_f32_16x16x32_bf16 v[106:109], v[142:145], v[240:243], v[106:109]
	v_mfma_f32_16x16x32_bf16 v[94:97], v[134:137], v[248:251], v[94:97]
	v_mfma_f32_16x16x32_bf16 v[90:93], v[142:145], v[248:251], v[90:93]
	v_mfma_f32_16x16x32_bf16 v[78:81], v[134:137], v[188:191], v[78:81]
	v_mfma_f32_16x16x32_bf16 v[74:77], v[142:145], v[188:191], v[74:77]
	s_setprio 0
	s_setprio 1
	v_mfma_f32_16x16x32_bf16 v[118:121], v[158:161], v[200:203], v[118:121]
	v_mfma_f32_16x16x32_bf16 v[114:117], v[182:185], v[200:203], v[114:117]
	v_mfma_f32_16x16x32_bf16 v[102:105], v[158:161], v[208:211], v[102:105]
	v_mfma_f32_16x16x32_bf16 v[98:101], v[182:185], v[208:211], v[98:101]
	v_mfma_f32_16x16x32_bf16 v[86:89], v[158:161], v[244:247], v[86:89]
	v_mfma_f32_16x16x32_bf16 v[82:85], v[182:185], v[244:247], v[82:85]
	v_mfma_f32_16x16x32_bf16 v[70:73], v[158:161], v[218:221], v[70:73]
	v_mfma_f32_16x16x32_bf16 v[66:69], v[182:185], v[218:221], v[66:69]
	v_mfma_f32_16x16x32_bf16 v[118:121], v[176:179], v[204:207], v[118:121]
	v_mfma_f32_16x16x32_bf16 v[114:117], v[196:199], v[204:207], v[114:117]
	v_mfma_f32_16x16x32_bf16 v[102:105], v[176:179], v[240:243], v[102:105]
	v_mfma_f32_16x16x32_bf16 v[98:101], v[196:199], v[240:243], v[98:101]
	v_mfma_f32_16x16x32_bf16 v[86:89], v[176:179], v[248:251], v[86:89]
	v_mfma_f32_16x16x32_bf16 v[82:85], v[196:199], v[248:251], v[82:85]
	v_mfma_f32_16x16x32_bf16 v[70:73], v[176:179], v[188:191], v[70:73]
	v_mfma_f32_16x16x32_bf16 v[66:69], v[196:199], v[188:191], v[66:69]
	s_setprio 0
	s_barrier
	s_mov_b32 m0, s45
	v_lshl_add_u64 v[168:169], s[30:31], 0, v[148:149]
	s_add_u32 s62, s30, 0x40000
	ds_read_b128 v[188:191], v165 offset:16384
	ds_read_b128 v[200:203], v165 offset:17408
	ds_read_b128 v[204:207], v165 offset:18432
	ds_read_b128 v[208:211], v165 offset:19456
	ds_read_b128 v[218:221], v165 offset:20480
	ds_read_b128 v[240:243], v165 offset:21504
	ds_read_b128 v[244:247], v165 offset:22528
	ds_read_b128 v[248:251], v165 offset:23552
	global_load_lds_dwordx4 v[168:169], off
	v_lshl_add_u64 v[172:173], s[30:31], 0, v[152:153]
	s_mov_b32 m0, s46
	s_addc_u32 s63, s31, 0
	global_load_lds_dwordx4 v[172:173], off
	v_lshl_add_u64 v[212:213], s[62:63], 0, v[148:149]
	s_mov_b32 m0, s47
	v_lshl_add_u64 v[222:223], s[40:41], 0, v[150:151]
	global_load_lds_dwordx4 v[212:213], off
	v_lshl_add_u64 v[212:213], s[62:63], 0, v[152:153]
	s_mov_b32 m0, s48
	s_nop 0
	global_load_lds_dwordx4 v[212:213], off
	v_lshl_add_u64 v[212:213], s[40:41], 0, v[146:147]
	s_mov_b32 m0, s44
	s_nop 0
	global_load_lds_dwordx4 v[212:213], off
	s_mov_b32 m0, s49
	s_nop 0
	global_load_lds_dwordx4 v[222:223], off
	s_cmp_eq_u32 s100, 0
	s_cbranch_scc1 .Lin_w8_1
	s_add_i32 s100, s100, -1
	s_cmp_eq_u32 s101, 24
	s_cbranch_scc1 .Lin_w24_1
	s_waitcnt vmcnt(16)
	s_branch .Lin_wd_1

; #define PG8_STAGE(bufoff, gbase, voff) do { _Pragma("unroll") for (int _i = 0; _i < 2; ++_i) \
;         __builtin_amdgcn_global_load_lds((const unsigned*)((const char*)(gbase) + (voff)[_i]), (PG8_LAS unsigned*)(lds + (bufoff) + ldsw + _i * 8192), 16, 0, 0); } while (0)
; #define PG8_LDA(dst, b, h) do { _Pragma("unroll") for (int m = 0; m < 4; ++m) _Pragma("unroll") for (int k = 0; k < 2; ++k) dst[m][k] = *(const PG8_LAS bf16x8*)(lds + PG8_SA(b, h) + aoff + m * 2048 + k * 1024); } while (0)
; #define PG8_LDB(dst, b, h) do { _Pragma("unroll") for (int n = 0; n < 2; ++n) _Pragma("unroll") for (int k = 0; k < 2; ++k) dst[n][k] = *(const PG8_LAS bf16x8*)(lds + PG8_SB(b, h) + boff + n * 2048 + k * 1024); } while (0)
; #define PG8_MMA(ai, bj, At, Bt) do { __builtin_amdgcn_s_setprio(1); _Pragma("unroll") for (int m = 0; m < 4; ++m) _Pragma("unroll") for (int n = 0; n < 2; ++n) _Pragma("unroll") for (int k = 0; k < 2; ++k) \
;         acc[ai][bj][m][n] = __builtin_amdgcn_mfma_f32_16x16x32_bf16(Bt[n][k], At[m][k], acc[ai][bj][m][n], 0, 0, 0); __builtin_amdgcn_s_setprio(0); } while (0)
; #define PG8_WAIT_V(n) asm volatile("s_waitcnt vmcnt(" #n ")" ::: "memory")
; #define PG8_WAIT_L(n) asm volatile("s_waitcnt lgkmcnt(" #n ")" ::: "memory")
; #define PG8_BAR __builtin_amdgcn_s_barrier()
; #define PG8_SCHED __builtin_amdgcn_sched_barrier(0)
; template <class Epi, class Sched, bool ALIGN_EPI = false, bool SP2 = false>
; __device__ __forceinline__ void gemm_phase(PG8_LAS unsigned char* lds, const Gemm g, const Sched& S, const Epi& E, const int tid) {
;     ...
;             PG8_WAIT_V(8); PG8_WAIT_L(0); PG8_BAR; PG8_MMA(1, 0, At, B0); PG8_MMA(1, 1, At, B1); PG8_BAR; PG8_SCHED;
;             PG8_LDB(B0, 1, 0); PG8_LDB(B1, 1, 1); PG8_SCHED; PG8_LDA(At, 1, 0); PG8_STAGE(PG8_SA(0, 1), a2 + hstepA, voffA);
;             PG8_WAIT_V(8); PG8_WAIT_L(0); PG8_BAR; PG8_MMA(0, 0, At, B0); PG8_MMA(0, 1, At, B1); PG8_BAR; PG8_SCHED;
.Lin_wd_1:
	s_waitcnt lgkmcnt(0)
	s_barrier
	s_setprio 1
	s_waitcnt lgkmcnt(0)
	v_mfma_f32_16x16x32_bf16 v[62:65], v[130:133], v[188:191], v[62:65]
	v_mfma_f32_16x16x32_bf16 v[58:61], v[138:141], v[188:191], v[58:61]
	v_mfma_f32_16x16x32_bf16 v[46:49], v[130:133], v[204:207], v[46:49]
	v_mfma_f32_16x16x32_bf16 v[42:45], v[138:141], v[204:207], v[42:45]
	v_mfma_f32_16x16x32_bf16 v[30:33], v[130:133], v[218:221], v[30:33]
	v_mfma_f32_16x16x32_bf16 v[26:29], v[138:141], v[218:221], v[26:29]
	v_mfma_f32_16x16x32_bf16 v[14:17], v[130:133], v[244:247], v[14:17]
	v_mfma_f32_16x16x32_bf16 v[10:13], v[138:141], v[244:247], v[10:13]
	v_mfma_f32_16x16x32_bf16 v[62:65], v[134:137], v[200:203], v[62:65]
	v_mfma_f32_16x16x32_bf16 v[58:61], v[142:145], v[200:203], v[58:61]
	v_mfma_f32_16x16x32_bf16 v[46:49], v[134:137], v[208:211], v[46:49]
	v_mfma_f32_16x16x32_bf16 v[42:45], v[142:145], v[208:211], v[42:45]
	v_mfma_f32_16x16x32_bf16 v[30:33], v[134:137], v[240:243], v[30:33]
	v_mfma_f32_16x16x32_bf16 v[26:29], v[142:145], v[240:243], v[26:29]
	v_mfma_f32_16x16x32_bf16 v[14:17], v[134:137], v[248:251], v[14:17]
	v_mfma_f32_16x16x32_bf16 v[10:13], v[142:145], v[248:251], v[10:13]
	s_setprio 0
	s_setprio 1
	v_mfma_f32_16x16x32_bf16 v[54:57], v[158:161], v[188:191], v[54:57]
	v_mfma_f32_16x16x32_bf16 v[50:53], v[182:185], v[188:191], v[50:53]
	v_mfma_f32_16x16x32_bf16 v[38:41], v[158:161], v[204:207], v[38:41]
	v_mfma_f32_16x16x32_bf16 v[34:37], v[182:185], v[204:207], v[34:37]
	v_mfma_f32_16x16x32_bf16 v[22:25], v[158:161], v[218:221], v[22:25]
	v_mfma_f32_16x16x32_bf16 v[18:21], v[182:185], v[218:221], v[18:21]
	v_mfma_f32_16x16x32_bf16 v[6:9], v[158:161], v[244:247], v[6:9]
	v_mfma_f32_16x16x32_bf16 v[2:5], v[182:185], v[244:247], v[2:5]
	v_mfma_f32_16x16x32_bf16 v[54:57], v[176:179], v[200:203], v[54:57]
	v_mfma_f32_16x16x32_bf16 v[50:53], v[196:199], v[200:203], v[50:53]
	v_mfma_f32_16x16x32_bf16 v[38:41], v[176:179], v[208:211], v[38:41]
	v_mfma_f32_16x16x32_bf16 v[34:37], v[196:199], v[208:211], v[34:37]
	v_mfma_f32_16x16x32_bf16 v[22:25], v[176:179], v[240:243], v[22:25]
	v_mfma_f32_16x16x32_bf16 v[18:21], v[196:199], v[240:243], v[18:21]
	v_mfma_f32_16x16x32_bf16 v[6:9], v[176:179], v[248:251], v[6:9]
	v_mfma_f32_16x16x32_bf16 v[2:5], v[196:199], v[248:251], v[2:5]
	s_setprio 0
	s_barrier
	v_or_b32_e32 v0, 0x18000, v167
	v_add_u32_e32 v134, 0x18400, v167
	ds_read_b128 v[130:133], v0
	ds_read_b128 v[134:137], v134
	v_add_u32_e32 v0, 0x18800, v167
	v_add_u32_e32 v142, 0x18c00, v167
	ds_read_b128 v[138:141], v0
	ds_read_b128 v[142:145], v142
	v_or_b32_e32 v0, 0x1c000, v167
	v_add_u32_e32 v162, 0x1c400, v167
	ds_read_b128 v[158:161], v0
	ds_read_b128 v[176:179], v162
	v_add_u32_e32 v0, 0x1c800, v167
	v_add_u32_e32 v162, 0x1cc00, v167
	ds_read_b128 v[182:185], v0
	ds_read_b128 v[188:191], v162
	s_add_u32 s40, s40, 0x40000
	s_addc_u32 s41, s41, 0
	s_mov_b32 m0, s50
	v_lshl_add_u64 v[228:229], s[40:41], 0, v[146:147]
	ds_read_b128 v[196:199], v165 offset:32768
	ds_read_b128 v[200:203], v165 offset:33792
	ds_read_b128 v[204:207], v165 offset:34816
	ds_read_b128 v[208:211], v165 offset:35840
	ds_read_b128 v[218:221], v165 offset:36864
	ds_read_b128 v[240:243], v165 offset:37888
	ds_read_b128 v[244:247], v165 offset:38912
	ds_read_b128 v[248:251], v165 offset:39936
	global_load_lds_dwordx4 v[228:229], off
	v_lshl_add_u64 v[228:229], s[40:41], 0, v[150:151]
	s_mov_b32 m0, s51
	s_nop 0
	global_load_lds_dwordx4 v[228:229], off
	s_waitcnt vmcnt(8)
	s_waitcnt lgkmcnt(0)
	s_barrier
	s_setprio 1
	s_waitcnt lgkmcnt(0)
	v_mfma_f32_16x16x32_bf16 v[126:129], v[130:133], v[196:199], v[126:129]
	v_mfma_f32_16x16x32_bf16 v[122:125], v[138:141], v[196:199], v[122:125]
	v_mfma_f32_16x16x32_bf16 v[110:113], v[130:133], v[204:207], v[110:113]
	v_mfma_f32_16x16x32_bf16 v[106:109], v[138:141], v[204:207], v[106:109]
	v_mfma_f32_16x16x32_bf16 v[94:97], v[130:133], v[218:221], v[94:97]
	v_mfma_f32_16x16x32_bf16 v[90:93], v[138:141], v[218:221], v[90:93]
	v_mfma_f32_16x16x32_bf16 v[78:81], v[130:133], v[244:247], v[78:81]
	v_mfma_f32_16x16x32_bf16 v[74:77], v[138:141], v[244:247], v[74:77]
	v_mfma_f32_16x16x32_bf16 v[126:129], v[134:137], v[200:203], v[126:129]
	v_mfma_f32_16x16x32_bf16 v[122:125], v[142:145], v[200:203], v[122:125]
	v_mfma_f32_16x16x32_bf16 v[110:113], v[134:137], v[208:211], v[110:113]
	v_mfma_f32_16x16x32_bf16 v[106:109], v[142:145], v[208:211], v[106:109]
	v_mfma_f32_16x16x32_bf16 v[94:97], v[134:137], v[240:243], v[94:97]
	v_mfma_f32_16x16x32_bf16 v[90:93], v[142:145], v[240:243], v[90:93]
	v_mfma_f32_16x16x32_bf16 v[78:81], v[134:137], v[248:251], v[78:81]
	v_mfma_f32_16x16x32_bf16 v[74:77], v[142:145], v[248:251], v[74:77]
	s_setprio 0
	s_setprio 1
	v_mfma_f32_16x16x32_bf16 v[118:121], v[158:161], v[196:199], v[118:121]
	v_mfma_f32_16x16x32_bf16 v[114:117], v[182:185], v[196:199], v[114:117]
	v_mfma_f32_16x16x32_bf16 v[102:105], v[158:161], v[204:207], v[102:105]
	v_mfma_f32_16x16x32_bf16 v[98:101], v[182:185], v[204:207], v[98:101]
	v_mfma_f32_16x16x32_bf16 v[86:89], v[158:161], v[218:221], v[86:89]
	v_mfma_f32_16x16x32_bf16 v[82:85], v[182:185], v[218:221], v[82:85]
	v_mfma_f32_16x16x32_bf16 v[70:73], v[158:161], v[244:247], v[70:73]
	v_mfma_f32_16x16x32_bf16 v[66:69], v[182:185], v[244:247], v[66:69]
	v_mfma_f32_16x16x32_bf16 v[118:121], v[176:179], v[200:203], v[118:121]
	v_mfma_f32_16x16x32_bf16 v[114:117], v[188:191], v[200:203], v[114:117]
	v_mfma_f32_16x16x32_bf16 v[102:105], v[176:179], v[208:211], v[102:105]
	v_mfma_f32_16x16x32_bf16 v[98:101], v[188:191], v[208:211], v[98:101]
	v_mfma_f32_16x16x32_bf16 v[86:89], v[176:179], v[240:243], v[86:89]
	v_mfma_f32_16x16x32_bf16 v[82:85], v[188:191], v[240:243], v[82:85]
	v_mfma_f32_16x16x32_bf16 v[70:73], v[176:179], v[248:251], v[70:73]
	v_mfma_f32_16x16x32_bf16 v[66:69], v[188:191], v[248:251], v[66:69]
	s_setprio 0
	s_barrier
; #define PG8_STAGE(bufoff, gbase, voff) do { _Pragma("unroll") for (int _i = 0; _i < 2; ++_i) \
;         __builtin_amdgcn_global_load_lds((const unsigned*)((const char*)(gbase) + (voff)[_i]), (PG8_LAS unsigned*)(lds + (bufoff) + ldsw + _i * 8192), 16, 0, 0); } while (0)
; #define PG8_LDA(dst, b, h) do { _Pragma("unroll") for (int m = 0; m < 4; ++m) _Pragma("unroll") for (int k = 0; k < 2; ++k) dst[m][k] = *(const PG8_LAS bf16x8*)(lds + PG8_SA(b, h) + aoff + m * 2048 + k * 1024); } while (0)
; #define PG8_MMA(ai, bj, At, Bt) do { __builtin_amdgcn_s_setprio(1); _Pragma("unroll") for (int m = 0; m < 4; ++m) _Pragma("unroll") for (int n = 0; n < 2; ++n) _Pragma("unroll") for (int k = 0; k < 2; ++k) \
;         acc[ai][bj][m][n] = __builtin_amdgcn_mfma_f32_16x16x32_bf16(Bt[n][k], At[m][k], acc[ai][bj][m][n], 0, 0, 0); __builtin_amdgcn_s_setprio(0); } while (0)
; #define PG8_WAIT_V(n) asm volatile("s_waitcnt vmcnt(" #n ")" ::: "memory")
; #define PG8_WAIT_L(n) asm volatile("s_waitcnt lgkmcnt(" #n ")" ::: "memory")
; #define PG8_BAR __builtin_amdgcn_s_barrier()
; #define PG8_SCHED __builtin_amdgcn_sched_barrier(0)
; template <class Epi, class Sched, bool ALIGN_EPI = false, bool SP2 = false>
; __device__ __forceinline__ void gemm_phase(PG8_LAS unsigned char* lds, const Gemm g, const Sched& S, const Epi& E, const int tid) {
;     ...
;             PG8_LDA(At, 1, 1); PG8_STAGE(PG8_SB(1, 0), b3, voffB); PG8_STAGE(PG8_SB(1, 1), b3 + hstep, voffB); PG8_STAGE(PG8_SA(1, 0), a3, voffA);
;             PG8_WAIT_V(8); PG8_WAIT_L(0); PG8_BAR; PG8_MMA(1, 0, At, B0); PG8_MMA(1, 1, At, B1); PG8_BAR; PG8_SCHED;
;     ...
;         if constexpr (ALIGN_EPI) { if (wr == 0) PG8_BAR; }
	s_mov_b32 m0, s52
	v_lshl_add_u64 v[168:169], v[168:169], 0, s[86:87]
	s_add_u32 s30, s30, 0x40080
	ds_read_b128 v[196:199], v165 offset:49152
	ds_read_b128 v[200:203], v165 offset:50176
	ds_read_b128 v[204:207], v165 offset:51200
	ds_read_b128 v[208:211], v165 offset:52224
	ds_read_b128 v[218:221], v165 offset:53248
	ds_read_b128 v[240:243], v165 offset:54272
	ds_read_b128 v[244:247], v165 offset:55296
	ds_read_b128 v[248:251], v165 offset:56320
	global_load_lds_dwordx4 v[168:169], off
	v_lshl_add_u64 v[168:169], v[172:173], 0, s[86:87]
	s_mov_b32 m0, s53
	s_addc_u32 s31, s31, 0
	global_load_lds_dwordx4 v[168:169], off
	v_lshl_add_u64 v[168:169], s[30:31], 0, v[148:149]
	s_mov_b32 m0, s56
	s_nop 0
	global_load_lds_dwordx4 v[168:169], off
	v_lshl_add_u64 v[168:169], s[30:31], 0, v[152:153]
	s_mov_b32 m0, s57
	s_nop 0
	global_load_lds_dwordx4 v[168:169], off
	v_lshl_add_u64 v[168:169], v[212:213], 0, s[86:87]
	s_mov_b32 m0, s54
	s_nop 0
	global_load_lds_dwordx4 v[168:169], off
	v_lshl_add_u64 v[168:169], v[222:223], 0, s[86:87]
	s_mov_b32 m0, s55
	s_nop 0
	global_load_lds_dwordx4 v[168:169], off
	s_waitcnt vmcnt(8)
	s_waitcnt lgkmcnt(0)
	s_barrier
	s_setprio 1
	s_waitcnt lgkmcnt(0)
	v_mfma_f32_16x16x32_bf16 v[62:65], v[130:133], v[196:199], v[62:65]
	v_mfma_f32_16x16x32_bf16 v[58:61], v[138:141], v[196:199], v[58:61]
	v_mfma_f32_16x16x32_bf16 v[46:49], v[130:133], v[204:207], v[46:49]
	v_mfma_f32_16x16x32_bf16 v[42:45], v[138:141], v[204:207], v[42:45]
	v_mfma_f32_16x16x32_bf16 v[30:33], v[130:133], v[218:221], v[30:33]
	v_mfma_f32_16x16x32_bf16 v[26:29], v[138:141], v[218:221], v[26:29]
	v_mfma_f32_16x16x32_bf16 v[14:17], v[130:133], v[244:247], v[14:17]
	v_mfma_f32_16x16x32_bf16 v[10:13], v[138:141], v[244:247], v[10:13]
	v_mfma_f32_16x16x32_bf16 v[62:65], v[134:137], v[200:203], v[62:65]
	v_mfma_f32_16x16x32_bf16 v[58:61], v[142:145], v[200:203], v[58:61]
	v_mfma_f32_16x16x32_bf16 v[46:49], v[134:137], v[208:211], v[46:49]
	v_mfma_f32_16x16x32_bf16 v[42:45], v[142:145], v[208:211], v[42:45]
	v_mfma_f32_16x16x32_bf16 v[30:33], v[134:137], v[240:243], v[30:33]
	v_mfma_f32_16x16x32_bf16 v[26:29], v[142:145], v[240:243], v[26:29]
	v_mfma_f32_16x16x32_bf16 v[14:17], v[134:137], v[248:251], v[14:17]
	v_mfma_f32_16x16x32_bf16 v[10:13], v[142:145], v[248:251], v[10:13]
	s_setprio 0
	s_setprio 1
	v_mfma_f32_16x16x32_bf16 v[54:57], v[158:161], v[196:199], v[54:57]
	v_mfma_f32_16x16x32_bf16 v[50:53], v[182:185], v[196:199], v[50:53]
	v_mfma_f32_16x16x32_bf16 v[38:41], v[158:161], v[204:207], v[38:41]
	v_mfma_f32_16x16x32_bf16 v[34:37], v[182:185], v[204:207], v[34:37]
	v_mfma_f32_16x16x32_bf16 v[22:25], v[158:161], v[218:221], v[22:25]
	v_mfma_f32_16x16x32_bf16 v[18:21], v[182:185], v[218:221], v[18:21]
	v_mfma_f32_16x16x32_bf16 v[6:9], v[158:161], v[244:247], v[6:9]
	v_mfma_f32_16x16x32_bf16 v[2:5], v[182:185], v[244:247], v[2:5]
	v_mfma_f32_16x16x32_bf16 v[54:57], v[176:179], v[200:203], v[54:57]
	v_mfma_f32_16x16x32_bf16 v[50:53], v[188:191], v[200:203], v[50:53]
	v_mfma_f32_16x16x32_bf16 v[38:41], v[176:179], v[208:211], v[38:41]
	v_mfma_f32_16x16x32_bf16 v[34:37], v[188:191], v[208:211], v[34:37]
	v_mfma_f32_16x16x32_bf16 v[22:25], v[176:179], v[240:243], v[22:25]
	v_mfma_f32_16x16x32_bf16 v[18:21], v[188:191], v[240:243], v[18:21]
	v_mfma_f32_16x16x32_bf16 v[6:9], v[176:179], v[248:251], v[6:9]
	v_mfma_f32_16x16x32_bf16 v[2:5], v[188:191], v[248:251], v[2:5]
	s_setprio 0
	s_barrier
	s_add_i32 s61, s61, 2
	s_add_u32 s59, s59, 0x100
	s_addc_u32 s60, s60, 0
	s_add_u32 s28, s28, 0x100
	s_addc_u32 s29, s29, 0
	s_cmp_gt_u32 s61, 13
	s_cbranch_scc0 .LBB0_556
	s_and_b64 vcc, exec, s[8:9]
	s_cbranch_vccz .LBB0_559
	s_barrier

; #define PG8_BAR __builtin_amdgcn_s_barrier()
; template <class Epi, class Sched, bool ALIGN_EPI = false, bool SP2 = false>
; __device__ __forceinline__ void gemm_phase(PG8_LAS unsigned char* lds, const Gemm g, const Sched& S, const Epi& E, const int tid) {
;     ...
;         if (!has_next) break;
; #pragma unroll
;         for (int a = 0; a < 2; ++a)
; #pragma unroll
;             for (int b = 0; b < 2; ++b)
; #pragma unroll
;                 for (int m = 0; m < 4; ++m)
; #pragma unroll
;                     for (int n = 0; n < 2; ++n) acc[a][b][m][n] = (f32x4){0.f, 0.f, 0.f, 0.f};
;         cur = nxt; cA = nA; cB = nB; ++ui;
;         if constexpr (ALIGN_EPI) { if (wr == 1) PG8_BAR; }
;     }
.LBB0_620:
	s_mov_b32 s100, 2
	s_cmp_eq_u32 s26, 13
	s_cselect_b32 s101, 16, 24
	s_andn2_b64 vcc, exec, s[38:39]
	s_mov_b64 s[4:5], -1
	s_cbranch_vccnz .LBB0_552
	s_andn2_b64 vcc, exec, s[0:1]
	s_cbranch_vccnz .LBB0_551
	s_barrier
	s_branch .LBB0_551
